# top-k latent unit: four affinity loads per thread issued together; wave-local bitonic stages handle a lane's two pairs in one LDS round trip
# speedup vs baseline: 1.0057x; 1.0057x over previous
.LBB0_1320:
	s_cmpk_lt_i32 s2, 0x100
	s_cselect_b64 s[18:19], -1, 0
	s_bfe_u32 s36, s2, 0x40004
	s_and_b32 s37, s2, 15
	s_cmpk_gt_i32 s2, 0xff
	s_cselect_b64 s[62:63], -1, 0
	s_and_b64 s[6:7], s[62:63], exec
	s_movk_i32 s6, 0x800
	s_cselect_b32 s35, 0x100, s6
	s_mul_i32 s34, s36, 0x900
	s_cselect_b32 s6, 0x800, 0
	s_add_i32 s34, s34, s6
	v_cmp_le_i32_e64 s[6:7], s35, v78
	v_cmp_gt_i32_e32 vcc, s35, v78
	s_barrier
	s_and_saveexec_b64 s[8:9], vcc
	s_cbranch_execz .LBB0_1323
	s_lshl_b32 s10, s37, 2
	s_add_u32 s10, s22, s10
	s_addc_u32 s11, s27, 0
	s_mov_b64 s[12:13], 0
	v_mov_b32_e32 v2, v83
	v_mov_b32_e32 v4, v82
	v_mov_b32_e32 v5, v78
	s_cmp_eq_u32 s35, 0x800
	s_cbranch_scc0 .LBB0_1322
	v_add_u32_e32 v6, s34, v5
	v_ashrrev_i32_e32 v7, 31, v6
	v_lshlrev_b64 v[6:7], 6, v[6:7]
	v_lshl_add_u64 v[6:7], s[10:11], 0, v[6:7]
	s_mov_b64 s[12:13], 0x8000
	v_lshl_add_u64 v[14:15], v[6:7], 0, s[12:13]
	v_lshl_add_u64 v[16:17], v[14:15], 0, s[12:13]
	v_lshl_add_u64 v[18:19], v[16:17], 0, s[12:13]
	v_add_u32_e32 v20, 0xfffffe00, v2
	v_add_u32_e32 v22, 0xfffffc00, v2
	v_add_u32_e32 v24, 0xfffffa00, v2
	global_load_dword v3, v[6:7], off
	global_load_dword v21, v[14:15], off
	global_load_dword v23, v[16:17], off
	global_load_dword v25, v[18:19], off
	s_waitcnt vmcnt(3)
	ds_write_b64 v4, v[2:3]
	s_waitcnt vmcnt(2)
	ds_write_b64 v4, v[20:21] offset:4096
	s_waitcnt vmcnt(1)
	ds_write_b64 v4, v[22:23] offset:8192
	s_waitcnt vmcnt(0)
	ds_write_b64 v4, v[24:25] offset:12288
	s_branch .LBB0_1323

.LBB0_1337:
	s_and_b64 vcc, exec, s[12:13]
	s_cbranch_vccz .LBB0_1327
	s_and_saveexec_b64 s[64:65], s[10:11]
	s_cbranch_execz .LBB0_1326
	s_cmp_eq_u32 s42, 0x80
	s_cbranch_scc0 .Lmy_tk_slow
	s_add_i32 s45, s44, -1
	s_sub_i32 s46, 0, s44
	v_add_u32_e32 v12, 64, v80
	v_and_b32_e32 v2, s46, v80
	v_and_b32_e32 v3, s45, v80
	v_lshl_or_b32 v2, v2, 1, v3
	v_add_u32_e32 v10, v2, v6
	v_or_b32_e32 v2, s44, v10
	v_lshl_add_u32 v8, v10, 3, 0
	v_lshl_add_u32 v9, v2, 3, 0
	v_and_b32_e32 v13, s46, v12
	v_and_b32_e32 v14, s45, v12
	v_lshl_or_b32 v13, v13, 1, v14
	v_add_u32_e32 v14, v13, v6
	v_or_b32_e32 v13, s44, v14
	v_lshl_add_u32 v15, v14, 3, 0
	v_lshl_add_u32 v16, v13, 3, 0
	ds_read_b64 v[2:3], v8
	ds_read_b64 v[4:5], v9
	ds_read_b64 v[18:19], v15
	ds_read_b64 v[20:21], v16
	v_and_b32_e32 v10, s43, v10
	v_cmp_ne_u32_e64 s[12:13], 0, v10
	v_and_b32_e32 v14, s43, v14
	v_cmp_ne_u32_e64 s[50:51], 0, v14
	s_waitcnt lgkmcnt(2)
	v_cmp_lt_u64_e32 vcc, v[2:3], v[4:5]
	s_xor_b64 s[12:13], vcc, s[12:13]
	s_waitcnt lgkmcnt(0)
	v_cmp_lt_u64_e32 vcc, v[18:19], v[20:21]
	s_xor_b64 s[50:51], vcc, s[50:51]
	s_mov_b64 s[66:67], exec
	s_and_b64 exec, s[66:67], s[12:13]
	ds_write_b64 v8, v[4:5]
	ds_write_b64 v9, v[2:3]
	s_and_b64 exec, s[66:67], s[50:51]
	ds_write_b64 v15, v[20:21]
	ds_write_b64 v16, v[18:19]
	s_mov_b64 exec, s[66:67]
	s_branch .LBB0_1326
.Lmy_tk_slow:
	s_add_i32 s45, s44, -1
	s_sub_i32 s46, 0, s44
	s_mov_b64 s[66:67], 0
	v_mov_b32_e32 v7, v80
	s_branch .LBB0_1341
